# mixer work-queue pop: thread 0 issues the fetch-add before the store-drain wait and the barrier, so the atomic round trip overlaps the drain and the barrier skew (stacked on v21)
# speedup vs baseline: 1.0042x; 1.0025x over previous
.LBB0_362:
	v_mov_b32_e32 v1, v0
	v_cmp_eq_u32_e32 vcc, 0, v1
	s_and_saveexec_b64 s[0:1], vcc
	s_cbranch_execz .Lqp_issued
	s_mov_b64 s[6:7], exec
	v_mbcnt_lo_u32_b32 v1, s6, 0
	v_mbcnt_hi_u32_b32 v1, s7, v1
	v_cmp_eq_u32_e32 vcc, 0, v1
	s_and_saveexec_b64 s[4:5], vcc
	s_cbranch_execz .Lqp_issued2
	s_bcnt1_i32_b64 s6, s[6:7]
	v_mov_b32_e32 v2, s6
	v_readlane_b32 s6, v236, 20
	v_readlane_b32 s7, v236, 21
	s_nop 4
	global_atomic_add v2, v3, v2, s[6:7] sc0

.Lqp_issued:
	s_or_b64 exec, exec, s[0:1]
	s_waitcnt vmcnt(0)
	s_barrier
	v_cmp_eq_u32_e32 vcc, 0, v0
	s_and_saveexec_b64 s[0:1], vcc
	s_cbranch_execz .LBB0_366
	v_readfirstlane_b32 s4, v2
	s_nop 1
	v_add_u32_e32 v1, s4, v1
	v_readlane_b32 s4, v239, 30
	s_nop 1
	v_mov_b32_e32 v2, s4
	ds_write_b32 v2, v1
